# grid barrier: all workgroups poll the top generation word (per-XCD generation hop removed)
# baseline (speedup 1.0000x reference)
; __device__ __forceinline__ unsigned xb_ld(unsigned* p)              { return __hip_atomic_load(p, __ATOMIC_RELAXED, __HIP_MEMORY_SCOPE_AGENT); }
; __device__ __forceinline__ unsigned xb_add(unsigned* p, unsigned v) { return __hip_atomic_fetch_add(p, v, __ATOMIC_RELAXED, __HIP_MEMORY_SCOPE_AGENT); }
; #define XB_SPIN(cond, bar) do { unsigned _sp = 0; while (cond) { __builtin_amdgcn_s_sleep(1); \
;     if ((++_sp & 255u) == 0u) { if (xb_ld(&(bar)[XB_TMO])) break; if (_sp > XB_SPIN_CAP) { atomicAdd(&(bar)[XB_TMO], 1u); break; } } } } while (0)
; __device__ __forceinline__ void xcd_barrier(const XcdBarrier& b) {
;     ...
;         const unsigned old = xb_add(&bar[XB_XSUB(b.x)], 1u);
;         const unsigned gen = old / nloc;
;         if (old + 1u == (gen + 1u) * nloc) {
;             __builtin_amdgcn_fence(__ATOMIC_RELEASE, "agent");
;             asm volatile("s_waitcnt vmcnt(0)" ::: "memory");
;             const unsigned og = xb_add(&bar[XB_TOP], 1u);
;             const unsigned tg = og / nx;
;             if (og + 1u == (tg + 1u) * nx) xb_add(&bar[XB_TOPGEN], 1u);
;             else XB_SPIN(xb_ld(&bar[XB_TOPGEN]) == tg, bar);
;             __builtin_amdgcn_fence(__ATOMIC_ACQUIRE, "agent");
;             xb_add(&bar[XB_XGEN(b.x)], 1u);
;             asm volatile("s_waitcnt vmcnt(0)" ::: "memory");
;         } else {
;             XB_SPIN(xb_ld(&bar[XB_XGEN(b.x)]) == gen, bar);
.LBB0_54:
	v_readlane_b32 s2, v246, 21
	s_lshl_b32 s2, s2, 8
	v_readlane_b32 s4, v246, 19
	v_readlane_b32 s5, v246, 20
	s_add_u32 s4, s4, s2
	s_addc_u32 s5, s5, 0
	v_mov_b32_e32 v2, 0x1000
	v_mov_b32_e32 v4, 1
	v_sub_u32_e32 v5, 0, v3
	global_atomic_add v4, v2, v4, s[4:5] offset:1024 sc0
	v_cvt_f32_u32_e32 v2, v3
	v_rcp_iflag_f32_e32 v2, v2
	s_nop 0
	v_mul_f32_e32 v2, 0x4f7ffffe, v2
	v_cvt_u32_f32_e32 v2, v2
	v_mul_lo_u32 v5, v5, v2
	v_mul_hi_u32 v5, v2, v5
	v_add_u32_e32 v2, v2, v5
	s_waitcnt vmcnt(0)
	v_mul_hi_u32 v2, v4, v2
	v_mul_lo_u32 v5, v2, v3
	v_sub_u32_e32 v5, v4, v5
	v_add_u32_e32 v6, 1, v2
	v_cmp_ge_u32_e32 vcc, v5, v3
	v_add_u32_e32 v4, 1, v4
	s_nop 0
	v_cndmask_b32_e32 v2, v2, v6, vcc
	v_sub_u32_e32 v6, v5, v3
	v_cndmask_b32_e32 v5, v5, v6, vcc
	v_add_u32_e32 v6, 1, v2
	v_cmp_ge_u32_e32 vcc, v5, v3
	s_nop 1
	v_cndmask_b32_e32 v2, v2, v6, vcc
	v_mul_lo_u32 v5, v3, v2
	v_add_u32_e32 v3, v5, v3
	v_cmp_ne_u32_e32 vcc, v4, v3
	s_and_saveexec_b64 s[2:3], vcc
	s_xor_b64 s[2:3], exec, s[2:3]
	s_cbranch_execz .LBB0_68
	s_waitcnt lgkmcnt(0)
	v_mov_b32_e32 v1, 0x7000
	global_load_dword v1, v1, s[92:93] offset:1280 sc1
	s_add_u32 s10, s92, 0x7500
	s_addc_u32 s11, s93, 0
	s_waitcnt vmcnt(0)
	v_cmp_eq_u32_e32 vcc, v1, v2
	s_and_saveexec_b64 s[6:7], vcc
	s_cbranch_execz .LBB0_67
	s_add_u32 s8, s92, 0x4200
	s_addc_u32 s9, s93, 0
	s_mov_b32 s22, 1
	s_mov_b64 s[12:13], 0
	v_mov_b32_e32 v1, 0
	s_branch .LBB0_58

; __device__ __forceinline__ unsigned xb_add(unsigned* p, unsigned v) { return __hip_atomic_fetch_add(p, v, __ATOMIC_RELAXED, __HIP_MEMORY_SCOPE_AGENT); }
; __device__ __forceinline__ void xcd_barrier(const XcdBarrier& b) {
;     ...
;             __builtin_amdgcn_fence(__ATOMIC_ACQUIRE, "agent");
;             xb_add(&bar[XB_XGEN(b.x)], 1u);
;             asm volatile("s_waitcnt vmcnt(0)" ::: "memory");
.LBB0_85:
	s_or_b64 exec, exec, s[2:3]
	v_mov_b32_e32 v1, 0x2000
	v_mov_b32_e32 v2, 1
	s_waitcnt vmcnt(0)
	buffer_inv sc1
	s_waitcnt vmcnt(0)

; __device__ __forceinline__ unsigned xb_ld(unsigned* p)              { return __hip_atomic_load(p, __ATOMIC_RELAXED, __HIP_MEMORY_SCOPE_AGENT); }
; __device__ __forceinline__ unsigned xb_add(unsigned* p, unsigned v) { return __hip_atomic_fetch_add(p, v, __ATOMIC_RELAXED, __HIP_MEMORY_SCOPE_AGENT); }
; #define XB_SPIN(cond, bar) do { unsigned _sp = 0; while (cond) { __builtin_amdgcn_s_sleep(1); \
;     if ((++_sp & 255u) == 0u) { if (xb_ld(&(bar)[XB_TMO])) break; if (_sp > XB_SPIN_CAP) { atomicAdd(&(bar)[XB_TMO], 1u); break; } } } } while (0)
; __device__ __forceinline__ void xcd_barrier(const XcdBarrier& b) {
;     ...
;         const unsigned old = xb_add(&bar[XB_XSUB(b.x)], 1u);
;         const unsigned gen = old / nloc;
;         if (old + 1u == (gen + 1u) * nloc) {
;             __builtin_amdgcn_fence(__ATOMIC_RELEASE, "agent");
;             asm volatile("s_waitcnt vmcnt(0)" ::: "memory");
;             const unsigned og = xb_add(&bar[XB_TOP], 1u);
;             const unsigned tg = og / nx;
;             if (og + 1u == (tg + 1u) * nx) xb_add(&bar[XB_TOPGEN], 1u);
;             else XB_SPIN(xb_ld(&bar[XB_TOPGEN]) == tg, bar);
;             __builtin_amdgcn_fence(__ATOMIC_ACQUIRE, "agent");
;             xb_add(&bar[XB_XGEN(b.x)], 1u);
;             asm volatile("s_waitcnt vmcnt(0)" ::: "memory");
;         } else {
;             XB_SPIN(xb_ld(&bar[XB_XGEN(b.x)]) == gen, bar);
.LBB0_262:
	v_readlane_b32 s2, v246, 21
	s_lshl_b32 s2, s2, 8
	v_readlane_b32 s8, v246, 19
	v_readlane_b32 s9, v246, 20
	s_add_u32 s8, s8, s2
	s_addc_u32 s9, s9, 0
	v_mov_b32_e32 v2, 0x1000
	v_mov_b32_e32 v4, 1
	v_sub_u32_e32 v5, 0, v3
	global_atomic_add v4, v2, v4, s[8:9] offset:1024 sc0
	v_cvt_f32_u32_e32 v2, v3
	v_rcp_iflag_f32_e32 v2, v2
	s_nop 0
	v_mul_f32_e32 v2, 0x4f7ffffe, v2
	v_cvt_u32_f32_e32 v2, v2
	v_mul_lo_u32 v5, v5, v2
	v_mul_hi_u32 v5, v2, v5
	v_add_u32_e32 v2, v2, v5
	s_waitcnt vmcnt(0)
	v_mul_hi_u32 v2, v4, v2
	v_mul_lo_u32 v5, v2, v3
	v_sub_u32_e32 v5, v4, v5
	v_add_u32_e32 v6, 1, v2
	v_cmp_ge_u32_e32 vcc, v5, v3
	v_add_u32_e32 v4, 1, v4
	s_nop 0
	v_cndmask_b32_e32 v2, v2, v6, vcc
	v_sub_u32_e32 v6, v5, v3
	v_cndmask_b32_e32 v5, v5, v6, vcc
	v_add_u32_e32 v6, 1, v2
	v_cmp_ge_u32_e32 vcc, v5, v3
	s_nop 1
	v_cndmask_b32_e32 v2, v2, v6, vcc
	v_mul_lo_u32 v5, v3, v2
	v_add_u32_e32 v3, v5, v3
	v_cmp_ne_u32_e32 vcc, v4, v3
	s_and_saveexec_b64 s[2:3], vcc
	s_xor_b64 s[2:3], exec, s[2:3]
	s_cbranch_execz .LBB0_276
	s_waitcnt lgkmcnt(0)
	v_mov_b32_e32 v1, 0x7000
	global_load_dword v1, v1, s[92:93] offset:1280 sc1
	s_add_u32 s14, s92, 0x7500
	s_addc_u32 s15, s93, 0
	s_waitcnt vmcnt(0)
	v_cmp_eq_u32_e32 vcc, v1, v2
	s_and_saveexec_b64 s[10:11], vcc
	s_cbranch_execz .LBB0_275
	s_add_u32 s12, s92, 0x4200
	s_addc_u32 s13, s93, 0
	s_mov_b32 s26, 1
	s_mov_b64 s[16:17], 0
	v_mov_b32_e32 v1, 0
	s_branch .LBB0_266

; __device__ __forceinline__ unsigned xb_ld(unsigned* p)              { return __hip_atomic_load(p, __ATOMIC_RELAXED, __HIP_MEMORY_SCOPE_AGENT); }
; __device__ __forceinline__ unsigned xb_add(unsigned* p, unsigned v) { return __hip_atomic_fetch_add(p, v, __ATOMIC_RELAXED, __HIP_MEMORY_SCOPE_AGENT); }
; #define XB_SPIN(cond, bar) do { unsigned _sp = 0; while (cond) { __builtin_amdgcn_s_sleep(1); \
;     if ((++_sp & 255u) == 0u) { if (xb_ld(&(bar)[XB_TMO])) break; if (_sp > XB_SPIN_CAP) { atomicAdd(&(bar)[XB_TMO], 1u); break; } } } } while (0)
; __device__ __forceinline__ void xcd_barrier(const XcdBarrier& b) {
;     ...
;         const unsigned old = xb_add(&bar[XB_XSUB(b.x)], 1u);
;         const unsigned gen = old / nloc;
;         if (old + 1u == (gen + 1u) * nloc) {
;             __builtin_amdgcn_fence(__ATOMIC_RELEASE, "agent");
;             asm volatile("s_waitcnt vmcnt(0)" ::: "memory");
;             const unsigned og = xb_add(&bar[XB_TOP], 1u);
;             const unsigned tg = og / nx;
;             if (og + 1u == (tg + 1u) * nx) xb_add(&bar[XB_TOPGEN], 1u);
;             else XB_SPIN(xb_ld(&bar[XB_TOPGEN]) == tg, bar);
;             __builtin_amdgcn_fence(__ATOMIC_ACQUIRE, "agent");
;             xb_add(&bar[XB_XGEN(b.x)], 1u);
;             asm volatile("s_waitcnt vmcnt(0)" ::: "memory");
;         } else {
;             XB_SPIN(xb_ld(&bar[XB_XGEN(b.x)]) == gen, bar);
;             __builtin_amdgcn_fence(__ATOMIC_ACQUIRE, "agent");
;             asm volatile("s_waitcnt vmcnt(0)" ::: "memory");
;         }
.LBB0_1047:
	v_readlane_b32 s2, v246, 21
	s_lshl_b32 s2, s2, 8
	v_readlane_b32 s4, v246, 19
	v_readlane_b32 s5, v246, 20
	s_add_u32 s2, s4, s2
	s_addc_u32 s3, s5, 0
	v_mov_b32_e32 v2, 0x1000
	v_mov_b32_e32 v4, 1
	global_atomic_add v4, v2, v4, s[2:3] offset:1024 sc0
	v_cvt_f32_u32_e32 v2, v3
	v_sub_u32_e32 v5, 0, v3
	v_rcp_iflag_f32_e32 v2, v2
	s_nop 0
	v_mul_f32_e32 v2, 0x4f7ffffe, v2
	v_cvt_u32_f32_e32 v2, v2
	v_mul_lo_u32 v5, v5, v2
	v_mul_hi_u32 v5, v2, v5
	v_add_u32_e32 v2, v2, v5
	s_waitcnt vmcnt(0)
	v_mul_hi_u32 v2, v4, v2
	v_mul_lo_u32 v5, v2, v3
	v_sub_u32_e32 v5, v4, v5
	v_add_u32_e32 v6, 1, v2
	v_cmp_ge_u32_e32 vcc, v5, v3
	v_add_u32_e32 v4, 1, v4
	s_nop 0
	v_cndmask_b32_e32 v2, v2, v6, vcc
	v_sub_u32_e32 v6, v5, v3
	v_cndmask_b32_e32 v5, v5, v6, vcc
	v_add_u32_e32 v6, 1, v2
	v_cmp_ge_u32_e32 vcc, v5, v3
	s_nop 1
	v_cndmask_b32_e32 v2, v2, v6, vcc
	v_mul_lo_u32 v5, v3, v2
	v_add_u32_e32 v3, v5, v3
	v_cmp_ne_u32_e32 vcc, v4, v3
	s_and_saveexec_b64 s[4:5], vcc
	s_xor_b64 s[4:5], exec, s[4:5]
	s_cbranch_execz .LBB0_1061
	s_waitcnt lgkmcnt(0)
	v_mov_b32_e32 v1, 0x7000
	global_load_dword v1, v1, s[92:93] offset:1280 sc1
	s_add_u32 s10, s92, 0x7500
	s_addc_u32 s11, s93, 0
	s_waitcnt vmcnt(0)
	v_cmp_eq_u32_e32 vcc, v1, v2
	s_and_saveexec_b64 s[6:7], vcc
	s_cbranch_execz .LBB0_1060
	s_add_u32 s8, s92, 0x4200
	s_addc_u32 s9, s93, 0
	s_mov_b32 s22, 1
	s_mov_b64 s[12:13], 0
	v_mov_b32_e32 v1, 0
	s_branch .LBB0_1051

; __device__ __forceinline__ unsigned xb_ld(unsigned* p)              { return __hip_atomic_load(p, __ATOMIC_RELAXED, __HIP_MEMORY_SCOPE_AGENT); }
; __device__ __forceinline__ unsigned xb_add(unsigned* p, unsigned v) { return __hip_atomic_fetch_add(p, v, __ATOMIC_RELAXED, __HIP_MEMORY_SCOPE_AGENT); }
; #define XB_SPIN(cond, bar) do { unsigned _sp = 0; while (cond) { __builtin_amdgcn_s_sleep(1); \
;     if ((++_sp & 255u) == 0u) { if (xb_ld(&(bar)[XB_TMO])) break; if (_sp > XB_SPIN_CAP) { atomicAdd(&(bar)[XB_TMO], 1u); break; } } } } while (0)
; __device__ __forceinline__ void xcd_barrier(const XcdBarrier& b) {
;     ...
;             const unsigned og = xb_add(&bar[XB_TOP], 1u);
;             const unsigned tg = og / nx;
;             if (og + 1u == (tg + 1u) * nx) xb_add(&bar[XB_TOPGEN], 1u);
;             else XB_SPIN(xb_ld(&bar[XB_TOPGEN]) == tg, bar);
;             __builtin_amdgcn_fence(__ATOMIC_ACQUIRE, "agent");
;             xb_add(&bar[XB_XGEN(b.x)], 1u);
;             asm volatile("s_waitcnt vmcnt(0)" ::: "memory");
;         } else {
;             XB_SPIN(xb_ld(&bar[XB_XGEN(b.x)]) == gen, bar);
;             __builtin_amdgcn_fence(__ATOMIC_ACQUIRE, "agent");
;             asm volatile("s_waitcnt vmcnt(0)" ::: "memory");
.LBB0_1078:
	s_or_b64 exec, exec, s[4:5]
	v_mov_b32_e32 v1, 0x2000
	v_mov_b32_e32 v2, 1
	s_waitcnt vmcnt(0)
	buffer_inv sc1
	s_waitcnt vmcnt(0)
